# speedup vs baseline: 1.0089x; 1.0019x over previous
.LBB1_55:
	s_or_saveexec_b64 s[24:25], s[24:25]
	v_mov_b32_e32 v116, 0
	v_lshlrev_b32_e32 v234, 1, v190
	v_lshlrev_b32_e32 v235, 1, v191
	v_mov_b32_e32 v117, 0
	v_mov_b32_e32 v166, 0
	v_mov_b32_e32 v167, 0
	v_mov_b32_e32 v150, 0
	v_mov_b32_e32 v151, 0
	v_mov_b32_e32 v152, 0
	v_mov_b32_e32 v153, 0
	v_mov_b32_e32 v174, 0
	v_mov_b32_e32 v175, 0
	v_mov_b32_e32 v172, 0
	v_mov_b32_e32 v173, 0
	s_xor_b64 exec, exec, s[24:25]
	s_cbranch_execz .LBB1_57
	s_lshl_b32 s42, s46, 1
	v_add_u32_e32 v115, s42, v199
	v_mad_u32_u24 v176, v233, s3, v227
	v_mov_b32_e32 v115, s54
	v_mad_u32_u24 v162, v233, s53, v115
	v_add3_u32 v115, v162, v234, v235
	ds_read_b64 v[132:133], v115 offset:80
	v_mad_u32_u24 v115, v233, s52, v198
	ds_read_b128 v[150:153], v115 offset:60416
	v_mov_b32_e32 v115, s56
	s_waitcnt lgkmcnt(5)
	v_mfma_f32_16x16x32_bf16 v[240:243], v[86:89], v[146:149], 0
	s_waitcnt lgkmcnt(2)
	v_mfma_f32_16x16x32_bf16 v[124:127], v[124:127], v[138:141], 0
	v_mfma_f32_16x16x32_bf16 v[116:119], v[250:253], v[146:149], v[120:123]
	v_mfma_f32_16x16x32_bf16 v[118:121], v[246:249], v[142:145], v[116:119]
	v_mfma_f32_16x16x32_bf16 v[122:125], v[128:131], v[134:137], v[124:127]
	s_nop 0
	s_waitcnt lgkmcnt(1)
	v_lshlrev_b32_e32 v116, 16, v132
	v_and_b32_e32 v117, 0xffff0000, v132
	v_lshlrev_b32_e32 v166, 16, v133
	v_and_b32_e32 v167, 0xffff0000, v133
	s_nop 2
	v_add_f32_e32 v172, v120, v124
	v_add_f32_e32 v173, v121, v125
	v_add_f32_e32 v174, v118, v122
	v_add_f32_e32 v175, v119, v123
	v_sub_f32_e32 v119, 1.0, v117
	v_sub_f32_e32 v118, 1.0, v116
	v_sub_f32_e32 v121, 1.0, v167
	v_sub_f32_e32 v120, 1.0, v166
	v_mul_f32_e32 v120, v172, v120
	v_mul_f32_e32 v121, v173, v121
	v_mul_f32_e32 v118, v174, v118
	v_mul_f32_e32 v119, v175, v119
	s_waitcnt lgkmcnt(0)
	v_fma_f32 v122, v152, v166, v120
	v_fma_f32 v123, v153, v167, v121
	v_fma_f32 v124, v150, v116, v118
	v_fma_f32 v125, v151, v117, v119
	v_mfma_f32_16x16x32_bf16 v[118:121], v[2:5], v[146:149], 0
	v_cndmask_b32_e64 v115, v123, v115, s[14:15]
	v_cndmask_b32_e64 v123, v122, v122, s[14:15]
	v_cndmask_b32_e64 v122, v125, v125, s[14:15]
	v_cndmask_b32_e64 v124, v124, v124, s[14:15]
	v_cvt_pk_bf16_f32 v122, v124, v122
	v_cvt_pk_bf16_f32 v123, v123, v115
	ds_write_b64 v200, v[122:123] offset:58112
	s_and_saveexec_b64 s[72:73], s[18:19]
	v_mov_b32_e32 v115, 0xe380
	ds_add_u32 v115, v115
	s_or_b64 exec, exec, s[72:73]
	v_mfma_f32_16x16x32_bf16 v[118:121], v[6:9], v[142:145], v[118:121]
	v_lshl_add_u32 v115, v192, 1, v162
	ds_read_b128 v[130:133], v115 offset:128
	ds_read_b128 v[236:239], v176 offset:2304
	v_add_u32_e32 v115, s42, v228
	ds_read_b128 v[162:165], v115 offset:39168
	ds_read_b128 v[244:247], v115 offset:39232
	v_mfma_f32_16x16x32_bf16 v[118:121], v[10:13], v[138:141], v[118:121]
	v_mfma_f32_16x16x32_bf16 v[118:121], v[14:17], v[134:137], v[118:121]
	s_waitcnt lgkmcnt(1)
	v_mfma_f32_16x16x32_bf16 v[162:165], v[162:165], v[236:239], 0
	ds_read_b128 v[236:239], v176 offset:2368
	v_mfma_f32_16x16x32_bf16 v[126:129], v[26:29], v[130:133], v[118:121]
	v_mfma_f32_16x16x32_bf16 v[118:121], v[30:33], v[146:149], 0
	v_mfma_f32_16x16x32_bf16 v[122:125], v[58:61], v[146:149], 0
	v_mfma_f32_16x16x32_bf16 v[118:121], v[34:37], v[142:145], v[118:121]
	v_mfma_f32_16x16x32_bf16 v[122:125], v[62:65], v[142:145], v[122:125]
	s_waitcnt lgkmcnt(0)
	v_mfma_f32_16x16x32_bf16 v[162:165], v[244:247], v[236:239], v[162:165]
	v_mov_b32_e32 v246, 0xe380
	ds_read_b32 v246, v246
	v_mfma_f32_16x16x32_bf16 v[236:239], v[90:93], v[142:145], v[240:243]
	v_mfma_f32_16x16x32_bf16 v[118:121], v[38:41], v[138:141], v[118:121]
	s_nop 5
	v_med3_f32 v115, v162, s55, 0
	v_exp_f32_e32 v162, v115
	v_med3_f32 v115, v163, s55, 0
	v_mfma_f32_16x16x32_bf16 v[122:125], v[66:69], v[138:141], v[122:125]
	v_exp_f32_e32 v163, v115
	v_med3_f32 v115, v164, s55, 0
	v_exp_f32_e32 v164, v115
	v_mfma_f32_16x16x32_bf16 v[236:239], v[94:97], v[138:141], v[236:239]
	v_med3_f32 v115, v165, s55, 0
	v_exp_f32_e32 v165, v115
	v_mfma_f32_16x16x32_bf16 v[118:121], v[42:45], v[134:137], v[118:121]
	v_mfma_f32_16x16x32_bf16 v[122:125], v[70:73], v[134:137], v[122:125]
	v_mfma_f32_16x16x32_bf16 v[236:239], v[98:101], v[134:137], v[236:239]
	v_mfma_f32_16x16x32_bf16 v[118:121], v[54:57], v[130:133], v[118:121]
	v_mfma_f32_16x16x32_bf16 v[122:125], v[82:85], v[130:133], v[122:125]
	v_mfma_f32_16x16x32_bf16 v[130:133], v[110:113], v[130:133], v[236:239]

.Lpoll_done_0:
	ds_read_b128 v[142:145], v202 offset:58112
	ds_read_b128 v[146:149], v202 offset:58176
	v_mul_f32_e32 v176, v166, v152
	v_mul_f32_e32 v177, v167, v153
	v_mul_f32_e32 v240, v116, v150
	v_mul_f32_e32 v241, v117, v151
	s_waitcnt lgkmcnt(1)
	v_mfma_f32_16x16x32_bf16 v[134:137], v[134:137], v[142:145], 0
	v_add_f32_e64 v242, -v116, 1.0
	v_add_f32_e64 v243, -v117, 1.0
	s_waitcnt lgkmcnt(0)
	v_sub_f32_e32 v144, 1.0, v236
	v_sub_f32_e32 v145, 1.0, v237
	v_mfma_f32_16x16x32_bf16 v[140:143], v[138:141], v[146:149], 0
	s_nop 7
	v_add_f32_e32 v138, v136, v142
	v_add_f32_e32 v139, v137, v143
	v_add_f32_e32 v142, v134, v140
	v_add_f32_e32 v143, v135, v141
	v_mul_f32_e32 v136, v238, v138
	v_mul_f32_e32 v137, v239, v139
	v_mul_f32_e32 v134, v236, v142
	v_mul_f32_e32 v135, v237, v143
	v_sub_f32_e32 v140, 1.0, v238
	v_sub_f32_e32 v141, 1.0, v239
	v_fma_f32 v144, v174, v144, v134
	v_fma_f32 v145, v175, v145, v135
	v_fma_f32 v140, v172, v140, v136
	v_fma_f32 v141, v173, v141, v137
	v_sub_f32_e32 v136, 1.0, v166
	v_sub_f32_e32 v137, 1.0, v167
	v_fma_f32 v134, v242, v144, v240
	v_fma_f32 v135, v243, v145, v241
	v_fma_f32 v136, v136, v140, v176
	v_fma_f32 v137, v137, v141, v177
	s_and_saveexec_b64 s[42:43], s[16:17]
	s_cbranch_execz .LBB1_71
	v_mov_b32_e32 v115, s56
	v_cndmask_b32_e64 v115, v137, v115, s[14:15]
	v_cndmask_b32_e64 v147, v136, v136, s[14:15]
	v_cndmask_b32_e64 v146, v135, v135, s[14:15]
	v_cndmask_b32_e64 v148, v134, v134, s[14:15]
	v_cvt_pk_bf16_f32 v146, v148, v146
	v_cvt_pk_bf16_f32 v147, v147, v115
	v_mad_u32_u24 v115, v233, s53, v204
	ds_write_b64 v115, v[146:147]

.LBB1_91:
	s_or_saveexec_b64 s[24:25], s[24:25]
	v_mov_b32_e32 v116, 0
	v_mov_b32_e32 v117, 0
	v_mov_b32_e32 v172, 0
	v_mov_b32_e32 v173, 0
	v_mov_b32_e32 v150, 0
	v_mov_b32_e32 v151, 0
	v_mov_b32_e32 v152, 0
	v_mov_b32_e32 v153, 0
	v_mov_b32_e32 v176, 0
	v_mov_b32_e32 v177, 0
	v_mov_b32_e32 v174, 0
	v_mov_b32_e32 v175, 0
	s_xor_b64 exec, exec, s[24:25]
	s_cbranch_execz .LBB1_93
	s_lshl_b32 s42, s46, 1
	v_add_u32_e32 v115, s42, v199
	v_mul_u32_u24_e32 v132, 0xe0, v233
	v_add_u32_e32 v115, s54, v132
	v_add_u32_e32 v162, 0xe00, v115
	v_add3_u32 v115, v162, v234, v235
	ds_read_b64 v[132:133], v115 offset:80
	v_mad_u32_u24 v115, v167, s52, v198
	ds_read_b128 v[150:153], v115 offset:60416
	s_waitcnt lgkmcnt(5)
	v_mfma_f32_16x16x32_bf16 v[240:243], v[86:89], v[146:149], 0
	s_waitcnt lgkmcnt(2)
	v_mfma_f32_16x16x32_bf16 v[116:119], v[250:253], v[146:149], v[120:123]
	v_mfma_f32_16x16x32_bf16 v[124:127], v[124:127], v[138:141], 0
	v_mfma_f32_16x16x32_bf16 v[118:121], v[246:249], v[142:145], v[116:119]
	v_mfma_f32_16x16x32_bf16 v[122:125], v[128:131], v[134:137], v[124:127]
	s_nop 0
	s_waitcnt lgkmcnt(1)
	v_lshlrev_b32_e32 v116, 16, v132
	v_and_b32_e32 v117, 0xffff0000, v132
	v_lshlrev_b32_e32 v172, 16, v133
	v_and_b32_e32 v173, 0xffff0000, v133
	v_mov_b32_e32 v115, s56
	s_nop 3
	v_add_f32_e32 v174, v120, v124
	v_add_f32_e32 v175, v121, v125
	v_add_f32_e32 v176, v118, v122
	v_add_f32_e32 v177, v119, v123
	v_sub_f32_e32 v119, 1.0, v117
	v_sub_f32_e32 v118, 1.0, v116
	v_sub_f32_e32 v121, 1.0, v173
	v_sub_f32_e32 v120, 1.0, v172
	v_mul_f32_e32 v120, v174, v120
	v_mul_f32_e32 v121, v175, v121
	v_mul_f32_e32 v118, v176, v118
	v_mul_f32_e32 v119, v177, v119
	s_waitcnt lgkmcnt(0)
	v_fma_f32 v122, v152, v172, v120
	v_fma_f32 v123, v153, v173, v121
	v_fma_f32 v124, v150, v116, v118
	v_fma_f32 v125, v151, v117, v119
	v_mfma_f32_16x16x32_bf16 v[118:121], v[2:5], v[146:149], 0
	v_cndmask_b32_e64 v115, v123, v115, s[14:15]
	v_cndmask_b32_e64 v123, v122, v122, s[14:15]
	v_cndmask_b32_e64 v122, v125, v125, s[14:15]
	v_cndmask_b32_e64 v124, v124, v124, s[14:15]
	v_cvt_pk_bf16_f32 v122, v124, v122
	v_cvt_pk_bf16_f32 v123, v123, v115
	ds_write_b64 v200, v[122:123] offset:58112
	s_and_saveexec_b64 s[72:73], s[18:19]
	v_mov_b32_e32 v115, 0xe380
	ds_add_u32 v115, v115
	s_or_b64 exec, exec, s[72:73]
	v_mfma_f32_16x16x32_bf16 v[118:121], v[6:9], v[142:145], v[118:121]
	v_lshl_add_u32 v115, v192, 1, v162
	ds_read_b128 v[130:133], v115 offset:128
	v_add_u32_e32 v115, s42, v228
	ds_read_b128 v[162:165], v115 offset:39168
	ds_read_b128 v[244:247], v115 offset:39232
	s_add_i32 s42, s33, 32
	s_and_b32 s42, s42, 0x60
	v_mfma_f32_16x16x32_bf16 v[118:121], v[10:13], v[138:141], v[118:121]
	v_or_b32_e32 v236, s42, v189
	v_mad_u32_u24 v248, v236, s3, v227
	ds_read_b128 v[236:239], v248
	v_mfma_f32_16x16x32_bf16 v[118:121], v[14:17], v[134:137], v[118:121]
	s_waitcnt lgkmcnt(0)
	v_mfma_f32_16x16x32_bf16 v[162:165], v[162:165], v[236:239], 0
	ds_read_b128 v[236:239], v248 offset:64
	v_mfma_f32_16x16x32_bf16 v[126:129], v[26:29], v[130:133], v[118:121]
	v_mfma_f32_16x16x32_bf16 v[118:121], v[30:33], v[146:149], 0
	v_mfma_f32_16x16x32_bf16 v[122:125], v[58:61], v[146:149], 0
	v_mfma_f32_16x16x32_bf16 v[118:121], v[34:37], v[142:145], v[118:121]
	v_mfma_f32_16x16x32_bf16 v[122:125], v[62:65], v[142:145], v[122:125]
	s_waitcnt lgkmcnt(0)
	v_mfma_f32_16x16x32_bf16 v[162:165], v[244:247], v[236:239], v[162:165]
	v_mov_b32_e32 v246, 0xe380
	ds_read_b32 v246, v246
	v_mfma_f32_16x16x32_bf16 v[236:239], v[90:93], v[142:145], v[240:243]
	v_mfma_f32_16x16x32_bf16 v[118:121], v[38:41], v[138:141], v[118:121]
	s_nop 5
	v_med3_f32 v115, v162, s55, 0
	v_exp_f32_e32 v162, v115
	v_med3_f32 v115, v163, s55, 0
	v_mfma_f32_16x16x32_bf16 v[122:125], v[66:69], v[138:141], v[122:125]
	v_exp_f32_e32 v163, v115
	v_med3_f32 v115, v164, s55, 0
	v_exp_f32_e32 v164, v115
	v_mfma_f32_16x16x32_bf16 v[236:239], v[94:97], v[138:141], v[236:239]
	v_med3_f32 v115, v165, s55, 0
	v_exp_f32_e32 v165, v115
	v_mfma_f32_16x16x32_bf16 v[118:121], v[42:45], v[134:137], v[118:121]
	v_mfma_f32_16x16x32_bf16 v[122:125], v[70:73], v[134:137], v[122:125]
	v_mfma_f32_16x16x32_bf16 v[236:239], v[98:101], v[134:137], v[236:239]
	v_mfma_f32_16x16x32_bf16 v[118:121], v[54:57], v[130:133], v[118:121]
	v_mfma_f32_16x16x32_bf16 v[122:125], v[82:85], v[130:133], v[122:125]
	v_mfma_f32_16x16x32_bf16 v[130:133], v[110:113], v[130:133], v[236:239]

.Lpoll_done_1:
	ds_read_b128 v[142:145], v202 offset:58112
	ds_read_b128 v[146:149], v202 offset:58176
	v_mul_f32_e32 v240, v172, v152
	v_mul_f32_e32 v241, v173, v153
	v_mul_f32_e32 v242, v116, v150
	v_mul_f32_e32 v243, v117, v151
	s_waitcnt lgkmcnt(1)
	v_mfma_f32_16x16x32_bf16 v[134:137], v[134:137], v[142:145], 0
	v_add_f32_e64 v244, -v116, 1.0
	v_add_f32_e64 v245, -v117, 1.0
	s_waitcnt lgkmcnt(0)
	v_sub_f32_e32 v144, 1.0, v236
	v_sub_f32_e32 v145, 1.0, v237
	v_mfma_f32_16x16x32_bf16 v[140:143], v[138:141], v[146:149], 0
	s_nop 7
	v_add_f32_e32 v138, v136, v142
	v_add_f32_e32 v139, v137, v143
	v_add_f32_e32 v142, v134, v140
	v_add_f32_e32 v143, v135, v141
	v_mul_f32_e32 v136, v238, v138
	v_mul_f32_e32 v137, v239, v139
	v_mul_f32_e32 v134, v236, v142
	v_mul_f32_e32 v135, v237, v143
	v_sub_f32_e32 v140, 1.0, v238
	v_sub_f32_e32 v141, 1.0, v239
	v_fma_f32 v144, v176, v144, v134
	v_fma_f32 v145, v177, v145, v135
	v_fma_f32 v140, v174, v140, v136
	v_fma_f32 v141, v175, v141, v137
	v_sub_f32_e32 v136, 1.0, v172
	v_sub_f32_e32 v137, 1.0, v173
	v_fma_f32 v134, v244, v144, v242
	v_fma_f32 v135, v245, v145, v243
	v_fma_f32 v136, v136, v140, v240
	v_fma_f32 v137, v137, v141, v241
	s_and_saveexec_b64 s[42:43], s[16:17]
	s_cbranch_execz .LBB1_107
	v_mov_b32_e32 v115, s56
	v_cndmask_b32_e64 v115, v137, v115, s[14:15]
	v_cndmask_b32_e64 v147, v136, v136, s[14:15]
	v_cndmask_b32_e64 v146, v135, v135, s[14:15]
	v_cndmask_b32_e64 v148, v134, v134, s[14:15]
	v_cvt_pk_bf16_f32 v146, v148, v146
	v_cvt_pk_bf16_f32 v147, v147, v115
	v_mad_u32_u24 v115, v167, s53, v204
	ds_write_b64 v115, v[146:147]

.LBB1_127:
	s_or_saveexec_b64 s[24:25], s[24:25]
	v_mov_b32_e32 v116, 0
	v_mov_b32_e32 v117, 0
	v_mov_b32_e32 v172, 0
	v_mov_b32_e32 v173, 0
	v_mov_b32_e32 v150, 0
	v_mov_b32_e32 v151, 0
	v_mov_b32_e32 v152, 0
	v_mov_b32_e32 v153, 0
	v_mov_b32_e32 v176, 0
	v_mov_b32_e32 v177, 0
	v_mov_b32_e32 v174, 0
	v_mov_b32_e32 v175, 0
	s_xor_b64 exec, exec, s[24:25]
	s_cbranch_execz .LBB1_129
	s_lshl_b32 s42, s46, 1
	v_add_u32_e32 v115, s42, v199
	v_mul_u32_u24_e32 v132, 0xe0, v167
	v_add_u32_e32 v115, s54, v132
	v_add_u32_e32 v162, 0xe00, v115
	v_add3_u32 v115, v162, v234, v235
	ds_read_b64 v[132:133], v115 offset:80
	v_mad_u32_u24 v115, v236, s52, v198
	ds_read_b128 v[150:153], v115 offset:60416
	s_waitcnt lgkmcnt(5)
	v_mfma_f32_16x16x32_bf16 v[242:245], v[86:89], v[146:149], 0
	s_waitcnt lgkmcnt(2)
	v_mfma_f32_16x16x32_bf16 v[116:119], v[250:253], v[146:149], v[120:123]
	v_mfma_f32_16x16x32_bf16 v[124:127], v[124:127], v[138:141], 0
	v_mfma_f32_16x16x32_bf16 v[118:121], v[246:249], v[142:145], v[116:119]
	v_mfma_f32_16x16x32_bf16 v[122:125], v[128:131], v[134:137], v[124:127]
	s_nop 0
	s_waitcnt lgkmcnt(1)
	v_lshlrev_b32_e32 v116, 16, v132
	v_and_b32_e32 v117, 0xffff0000, v132
	v_lshlrev_b32_e32 v172, 16, v133
	v_and_b32_e32 v173, 0xffff0000, v133
	v_mov_b32_e32 v115, s56
	s_nop 3
	v_add_f32_e32 v174, v120, v124
	v_add_f32_e32 v175, v121, v125
	v_add_f32_e32 v176, v118, v122
	v_add_f32_e32 v177, v119, v123
	v_sub_f32_e32 v119, 1.0, v117
	v_sub_f32_e32 v118, 1.0, v116
	v_sub_f32_e32 v121, 1.0, v173
	v_sub_f32_e32 v120, 1.0, v172
	v_mul_f32_e32 v120, v174, v120
	v_mul_f32_e32 v121, v175, v121
	v_mul_f32_e32 v118, v176, v118
	v_mul_f32_e32 v119, v177, v119
	s_waitcnt lgkmcnt(0)
	v_fma_f32 v122, v152, v172, v120
	v_fma_f32 v123, v153, v173, v121
	v_fma_f32 v124, v150, v116, v118
	v_fma_f32 v125, v151, v117, v119
	v_mfma_f32_16x16x32_bf16 v[118:121], v[2:5], v[146:149], 0
	v_cndmask_b32_e64 v115, v123, v115, s[14:15]
	v_cndmask_b32_e64 v123, v122, v122, s[14:15]
	v_cndmask_b32_e64 v122, v125, v125, s[14:15]
	v_cndmask_b32_e64 v124, v124, v124, s[14:15]
	v_cvt_pk_bf16_f32 v122, v124, v122
	v_cvt_pk_bf16_f32 v123, v123, v115
	ds_write_b64 v200, v[122:123] offset:58112
	s_and_saveexec_b64 s[72:73], s[18:19]
	v_mov_b32_e32 v115, 0xe380
	ds_add_u32 v115, v115
	s_or_b64 exec, exec, s[72:73]
	v_mfma_f32_16x16x32_bf16 v[118:121], v[6:9], v[142:145], v[118:121]
	v_lshl_add_u32 v115, v192, 1, v162
	ds_read_b128 v[130:133], v115 offset:128
	v_add_u32_e32 v115, s42, v228
	ds_read_b128 v[162:165], v115 offset:39168
	ds_read_b128 v[246:249], v115 offset:39232
	s_add_i32 s42, s33, 32
	s_and_b32 s42, s42, 0x60
	v_mfma_f32_16x16x32_bf16 v[118:121], v[10:13], v[138:141], v[118:121]
	v_or_b32_e32 v167, s42, v189
	v_mad_u32_u24 v167, v167, s3, v227
	ds_read_b128 v[238:241], v167 offset:2304
	v_mfma_f32_16x16x32_bf16 v[118:121], v[14:17], v[134:137], v[118:121]
	s_waitcnt lgkmcnt(0)
	v_mfma_f32_16x16x32_bf16 v[162:165], v[162:165], v[238:241], 0
	ds_read_b128 v[238:241], v167 offset:2368
	v_mfma_f32_16x16x32_bf16 v[126:129], v[26:29], v[130:133], v[118:121]
	v_mfma_f32_16x16x32_bf16 v[118:121], v[30:33], v[146:149], 0
	v_mfma_f32_16x16x32_bf16 v[122:125], v[58:61], v[146:149], 0
	v_mfma_f32_16x16x32_bf16 v[118:121], v[34:37], v[142:145], v[118:121]
	v_mfma_f32_16x16x32_bf16 v[122:125], v[62:65], v[142:145], v[122:125]
	s_waitcnt lgkmcnt(0)
	v_mfma_f32_16x16x32_bf16 v[162:165], v[246:249], v[238:241], v[162:165]
	v_mov_b32_e32 v246, 0xe380
	ds_read_b32 v246, v246
	v_mfma_f32_16x16x32_bf16 v[238:241], v[90:93], v[142:145], v[242:245]
	v_mfma_f32_16x16x32_bf16 v[118:121], v[38:41], v[138:141], v[118:121]
	s_nop 5
	v_med3_f32 v115, v162, s55, 0
	v_exp_f32_e32 v162, v115
	v_med3_f32 v115, v163, s55, 0
	v_mfma_f32_16x16x32_bf16 v[122:125], v[66:69], v[138:141], v[122:125]
	v_exp_f32_e32 v163, v115
	v_med3_f32 v115, v164, s55, 0
	v_exp_f32_e32 v164, v115
	v_mfma_f32_16x16x32_bf16 v[238:241], v[94:97], v[138:141], v[238:241]
	v_med3_f32 v115, v165, s55, 0
	v_exp_f32_e32 v165, v115
	v_mfma_f32_16x16x32_bf16 v[118:121], v[42:45], v[134:137], v[118:121]
	v_mfma_f32_16x16x32_bf16 v[122:125], v[70:73], v[134:137], v[122:125]
	v_mfma_f32_16x16x32_bf16 v[238:241], v[98:101], v[134:137], v[238:241]
	v_mfma_f32_16x16x32_bf16 v[118:121], v[54:57], v[130:133], v[118:121]
	v_mfma_f32_16x16x32_bf16 v[122:125], v[82:85], v[130:133], v[122:125]
	v_mfma_f32_16x16x32_bf16 v[130:133], v[110:113], v[130:133], v[238:241]

.Lpoll_done_2:
	ds_read_b128 v[142:145], v202 offset:58112
	ds_read_b128 v[146:149], v202 offset:58176
	v_mul_f32_e32 v242, v172, v152
	v_mul_f32_e32 v243, v173, v153
	v_mul_f32_e32 v244, v116, v150
	v_mul_f32_e32 v245, v117, v151
	s_waitcnt lgkmcnt(1)
	v_mfma_f32_16x16x32_bf16 v[134:137], v[134:137], v[142:145], 0
	v_add_f32_e64 v246, -v116, 1.0
	v_add_f32_e64 v247, -v117, 1.0
	s_waitcnt lgkmcnt(0)
	v_sub_f32_e32 v144, 1.0, v238
	v_sub_f32_e32 v145, 1.0, v239
	v_mfma_f32_16x16x32_bf16 v[140:143], v[138:141], v[146:149], 0
	s_nop 7
	v_add_f32_e32 v138, v136, v142
	v_add_f32_e32 v139, v137, v143
	v_add_f32_e32 v142, v134, v140
	v_add_f32_e32 v143, v135, v141
	v_mul_f32_e32 v136, v240, v138
	v_mul_f32_e32 v137, v241, v139
	v_mul_f32_e32 v134, v238, v142
	v_mul_f32_e32 v135, v239, v143
	v_sub_f32_e32 v140, 1.0, v240
	v_sub_f32_e32 v141, 1.0, v241
	v_fma_f32 v144, v176, v144, v134
	v_fma_f32 v145, v177, v145, v135
	v_fma_f32 v140, v174, v140, v136
	v_fma_f32 v141, v175, v141, v137
	v_sub_f32_e32 v136, 1.0, v172
	v_sub_f32_e32 v137, 1.0, v173
	v_fma_f32 v134, v246, v144, v244
	v_fma_f32 v135, v247, v145, v245
	v_fma_f32 v136, v136, v140, v242
	v_fma_f32 v137, v137, v141, v243
	s_and_saveexec_b64 s[42:43], s[16:17]
	s_cbranch_execz .LBB1_143
	v_mov_b32_e32 v115, s56
	v_cndmask_b32_e64 v115, v137, v115, s[14:15]
	v_cndmask_b32_e64 v147, v136, v136, s[14:15]
	v_cndmask_b32_e64 v146, v135, v135, s[14:15]
	v_cndmask_b32_e64 v148, v134, v134, s[14:15]
	v_cvt_pk_bf16_f32 v146, v148, v146
	v_cvt_pk_bf16_f32 v147, v147, v115
	v_mad_u32_u24 v115, v236, s53, v204
	ds_write_b64 v115, v[146:147]

.LBB1_165:
	s_or_saveexec_b64 s[42:43], s[42:43]
	v_cndmask_b32_e64 v115, 0, 1, s[24:25]
	v_mov_b32_e32 v117, 0
	v_cmp_ne_u32_e64 s[24:25], 1, v115
	v_mov_b32_e32 v116, 0
	v_mov_b32_e32 v177, 0
	v_mov_b32_e32 v176, 0
	v_mov_b32_e32 v153, 0
	v_mov_b32_e32 v152, 0
	v_mov_b32_e32 v151, 0
	v_mov_b32_e32 v150, 0
	v_mov_b32_e32 v173, 0
	v_mov_b32_e32 v172, 0
	v_mov_b32_e32 v175, 0
	v_mov_b32_e32 v174, 0
	s_xor_b64 exec, exec, s[42:43]
	s_cbranch_execz .LBB1_169
	v_lshl_add_u32 v115, s48, 1, v199
	v_mul_u32_u24_e32 v132, 0xe0, v236
	s_and_b64 vcc, exec, s[24:25]
	v_add_u32_e32 v115, s54, v132
	v_add_u32_e32 v132, 0xe00, v115
	v_add3_u32 v115, v132, v234, v235
	s_waitcnt lgkmcnt(0)
	v_mfma_f32_16x16x32_bf16 v[124:127], v[124:127], v[142:145], 0
	v_mfma_f32_16x16x32_bf16 v[116:119], v[250:253], v[134:137], v[120:123]
	v_mfma_f32_16x16x32_bf16 v[118:121], v[246:249], v[138:141], v[116:119]
	s_nop 2
	ds_read_b64 v[116:117], v115 offset:80
	v_mad_u32_u24 v115, v167, s52, v198
	ds_read_b128 v[150:153], v115 offset:60416
	v_mfma_f32_16x16x32_bf16 v[122:125], v[128:131], v[146:149], v[124:127]
	v_mov_b32_e32 v115, s56
	s_waitcnt lgkmcnt(1)
	v_lshlrev_b32_e32 v174, 16, v116
	v_and_b32_e32 v175, 0xffff0000, v116
	v_lshlrev_b32_e32 v172, 16, v117
	v_and_b32_e32 v173, 0xffff0000, v117
	s_nop 1
	v_add_f32_e32 v116, v120, v124
	v_add_f32_e32 v117, v121, v125
	v_add_f32_e32 v176, v118, v122
	v_add_f32_e32 v177, v119, v123
	v_sub_f32_e32 v119, 1.0, v173
	v_sub_f32_e32 v118, 1.0, v172
	v_sub_f32_e32 v121, 1.0, v175
	v_sub_f32_e32 v120, 1.0, v174
	v_mul_f32_e32 v120, v176, v120
	v_mul_f32_e32 v121, v177, v121
	v_mul_f32_e32 v118, v116, v118
	v_mul_f32_e32 v119, v117, v119
	s_waitcnt lgkmcnt(0)
	v_fma_f32 v124, v150, v174, v120
	v_fma_f32 v125, v151, v175, v121
	v_fma_f32 v122, v152, v172, v118
	v_fma_f32 v123, v153, v173, v119
	v_cndmask_b32_e64 v124, v124, v124, s[14:15]
	v_cndmask_b32_e64 v115, v123, v115, s[14:15]
	v_cndmask_b32_e64 v123, v122, v122, s[14:15]
	v_cndmask_b32_e64 v122, v125, v125, s[14:15]
	v_cvt_pk_bf16_f32 v122, v124, v122
	v_cvt_pk_bf16_f32 v123, v123, v115
	v_mfma_f32_16x16x32_bf16 v[118:121], v[2:5], v[134:137], 0
	ds_write_b64 v200, v[122:123] offset:58112
	s_and_saveexec_b64 s[72:73], s[18:19]
	v_mov_b32_e32 v115, 0xe380
	ds_add_u32 v115, v115
	s_or_b64 exec, exec, s[72:73]
	v_lshl_add_u32 v115, v192, 1, v132
	v_mfma_f32_16x16x32_bf16 v[122:125], v[30:33], v[134:137], 0
	ds_read_b128 v[130:133], v115 offset:128
	v_mfma_f32_16x16x32_bf16 v[126:129], v[58:61], v[134:137], 0
	v_mfma_f32_16x16x32_bf16 v[234:237], v[86:89], v[134:137], 0
	v_mfma_f32_16x16x32_bf16 v[118:121], v[6:9], v[138:141], v[118:121]
	v_mfma_f32_16x16x32_bf16 v[122:125], v[34:37], v[138:141], v[122:125]
	v_mfma_f32_16x16x32_bf16 v[126:129], v[62:65], v[138:141], v[126:129]
	v_mfma_f32_16x16x32_bf16 v[234:237], v[90:93], v[138:141], v[234:237]
	v_mfma_f32_16x16x32_bf16 v[118:121], v[10:13], v[142:145], v[118:121]
	v_mfma_f32_16x16x32_bf16 v[122:125], v[38:41], v[142:145], v[122:125]
	v_mfma_f32_16x16x32_bf16 v[126:129], v[66:69], v[142:145], v[126:129]
	v_mfma_f32_16x16x32_bf16 v[234:237], v[94:97], v[142:145], v[234:237]
	v_mfma_f32_16x16x32_bf16 v[118:121], v[14:17], v[146:149], v[118:121]
	v_mfma_f32_16x16x32_bf16 v[122:125], v[42:45], v[146:149], v[122:125]
	v_mfma_f32_16x16x32_bf16 v[126:129], v[70:73], v[146:149], v[126:129]
	v_mfma_f32_16x16x32_bf16 v[234:237], v[98:101], v[146:149], v[234:237]
	s_waitcnt lgkmcnt(0)
	v_mfma_f32_16x16x32_bf16 v[118:121], v[26:29], v[130:133], v[118:121]
	v_mov_b32_e32 v246, 0xe380
	ds_read_b32 v246, v246
	v_mfma_f32_16x16x32_bf16 v[122:125], v[54:57], v[130:133], v[122:125]
	v_mfma_f32_16x16x32_bf16 v[126:129], v[82:85], v[130:133], v[126:129]
	v_mfma_f32_16x16x32_bf16 v[130:133], v[110:113], v[130:133], v[234:237]
	s_cbranch_vccnz .LBB1_168
	v_lshl_add_u32 v115, s48, 1, v228
	ds_read_b128 v[162:165], v115 offset:39168
	s_add_i32 s44, s33, 64
	v_and_or_b32 v233, s44, 64, v189
	v_mad_u32_u24 v233, v233, s3, v227
	ds_read_b128 v[234:237], v115 offset:39232
	ds_read_b128 v[238:241], v233
	ds_read_b128 v[242:245], v233 offset:64
	s_waitcnt lgkmcnt(1)
	v_mfma_f32_16x16x32_bf16 v[162:165], v[162:165], v[238:241], 0
	s_waitcnt lgkmcnt(0)
	v_mfma_f32_16x16x32_bf16 v[162:165], v[234:237], v[242:245], v[162:165]
	s_nop 7
	v_med3_f32 v115, v162, s55, 0
	v_med3_f32 v163, v163, s55, 0
	v_med3_f32 v164, v164, s55, 0
	v_med3_f32 v165, v165, s55, 0
	v_exp_f32_e32 v162, v115
	v_exp_f32_e32 v163, v163
	v_exp_f32_e32 v164, v164
	v_exp_f32_e32 v165, v165

.Lpoll_done_3:
	ds_read_b128 v[142:145], v202 offset:58112
	ds_read_b128 v[146:149], v202 offset:58176
	v_mul_f32_e32 v238, v172, v152
	v_mul_f32_e32 v239, v173, v153
	v_mul_f32_e32 v240, v174, v150
	v_mul_f32_e32 v241, v175, v151
	s_waitcnt lgkmcnt(1)
	v_mfma_f32_16x16x32_bf16 v[134:137], v[134:137], v[142:145], 0
	v_add_f32_e64 v242, -v174, 1.0
	v_add_f32_e64 v243, -v175, 1.0
	s_waitcnt lgkmcnt(0)
	v_sub_f32_e32 v144, 1.0, v234
	v_sub_f32_e32 v145, 1.0, v235
	v_mfma_f32_16x16x32_bf16 v[140:143], v[138:141], v[146:149], 0
	s_nop 7
	v_add_f32_e32 v138, v136, v142
	v_add_f32_e32 v139, v137, v143
	v_add_f32_e32 v142, v134, v140
	v_add_f32_e32 v143, v135, v141
	v_mul_f32_e32 v136, v236, v138
	v_mul_f32_e32 v137, v237, v139
	v_mul_f32_e32 v134, v234, v142
	v_mul_f32_e32 v135, v235, v143
	v_sub_f32_e32 v140, 1.0, v236
	v_sub_f32_e32 v141, 1.0, v237
	v_fma_f32 v144, v176, v144, v134
	v_fma_f32 v145, v177, v145, v135
	v_fma_f32 v140, v116, v140, v136
	v_fma_f32 v141, v117, v141, v137
	v_sub_f32_e32 v136, 1.0, v172
	v_sub_f32_e32 v137, 1.0, v173
	v_fma_f32 v134, v242, v144, v240
	v_fma_f32 v135, v243, v145, v241
	v_fma_f32 v136, v136, v140, v238
	v_fma_f32 v137, v137, v141, v239
	s_and_saveexec_b64 s[44:45], s[16:17]
	s_cbranch_execz .LBB1_183
	v_mov_b32_e32 v115, s56
	v_cndmask_b32_e64 v115, v137, v115, s[14:15]
	v_cndmask_b32_e64 v147, v136, v136, s[14:15]
	v_cndmask_b32_e64 v146, v135, v135, s[14:15]
	v_cndmask_b32_e64 v148, v134, v134, s[14:15]
	v_cvt_pk_bf16_f32 v146, v148, v146
	v_cvt_pk_bf16_f32 v147, v147, v115
	v_mad_u32_u24 v115, v167, s53, v204
	ds_write_b64 v115, v[146:147]
